# GDN chain compute: four q.S chains, then scales, then att.v MFMAs interleaved (no padded waits); bit-identical
# speedup vs baseline: 1.0057x; 1.0012x over previous
; #define MFMA32(a, b, c) __builtin_amdgcn_mfma_f32_16x16x32_bf16((a), (b), (c), 0, 0, 0)
; __device__ void phase_gdn_chain(const Params& p, int l, char* smem, int vb, int nvb, int oz) {
;     ...
;                 ohave = need_o;
;                 if (need_o) {
;                     orow = c.rowbase + c.t0;
; #pragma unroll
;                     for (int mt = 0; mt < 4; ++mt) {
;                         f32x4 acc = {0.f, 0.f, 0.f, 0.f};
; #pragma unroll
;                         for (int s = 0; s < 2; ++s) acc = MFMA32(sf[s], qa[mt][s], acc);
;                         acc = acc * eGc[mt];
; #pragma unroll
;                         for (int s = 0; s < 2; ++s)
;                             if (!(dir ? (s == 0 && mt >= 2) : (s == 1 && mt < 2))) acc = MFMA32(vf[s], aa[mt][s], acc);
;                         onew[mt] = pack4(acc);
;                     }
;                 }
.LBB0_394:
	s_add_i32 s27, s26, -4
	s_and_b64 s[0:1], s[56:57], exec
	s_cselect_b32 s27, s27, s26
	s_cselect_b32 s0, 31, 3
	s_sub_i32 s31, s0, s27
	s_and_b64 s[0:1], s[44:45], exec
	s_cselect_b32 s0, s27, s31
	s_lshl_b32 s27, s0, 6
	s_ashr_i32 s31, s27, 31
	s_and_b64 s[0:1], s[56:57], exec
	s_cselect_b32 s1, s50, s24
	s_cselect_b32 s0, s51, s25
	s_add_u32 s54, s1, s27
	v_cvt_pk_bf16_f32 v156, v108, v109
	v_cvt_pk_bf16_f32 v157, v110, v111
	v_cvt_pk_bf16_f32 v158, v104, v105
	v_cvt_pk_bf16_f32 v159, v106, v107
	v_cvt_pk_bf16_f32 v160, v96, v97
	v_cvt_pk_bf16_f32 v161, v98, v99
	v_cvt_pk_bf16_f32 v162, v112, v113
	v_cvt_pk_bf16_f32 v163, v114, v115
	s_addc_u32 s55, s0, s31

; #define MFMA32(a, b, c) __builtin_amdgcn_mfma_f32_16x16x32_bf16((a), (b), (c), 0, 0, 0)
; __device__ void phase_gdn_chain(const Params& p, int l, char* smem, int vb, int nvb, int oz) {
;     ...
; #pragma unroll
;                 for (int mt = 0; mt < 4; ++mt) {
;                     f32x4 acc = S[mt] * gt;
; #pragma unroll
;                     for (int s = 0; s < 2; ++s) acc = MFMA32(ka[mt][s], vsf[s], acc);
;                     S[mt] = acc;
;                 }
;                 ohave = need_o;
;                 if (need_o) {
;                     orow = c.rowbase + c.t0;
; #pragma unroll
;                     for (int mt = 0; mt < 4; ++mt) {
;                         f32x4 acc = {0.f, 0.f, 0.f, 0.f};
; #pragma unroll
;                         for (int s = 0; s < 2; ++s) acc = MFMA32(sf[s], qa[mt][s], acc);
;                         acc = acc * eGc[mt];
; #pragma unroll
;                         for (int s = 0; s < 2; ++s)
;                             if (!(dir ? (s == 0 && mt >= 2) : (s == 1 && mt < 2))) acc = MFMA32(vf[s], aa[mt][s], acc);
;                         onew[mt] = pack4(acc);
;                     }
;                 }
.LBB0_408:
	v_pk_mul_f32 v[122:123], v[122:123], v[94:95]
	v_pk_mul_f32 v[120:121], v[120:121], v[92:93]
	v_pk_mul_f32 v[174:175], v[118:119], v[98:99]
	v_pk_mul_f32 v[118:119], v[116:117], v[96:97]
	v_cvt_pk_bf16_f32 v116, v120, v121
	v_cvt_pk_bf16_f32 v117, v122, v123
	v_cvt_pk_bf16_f32 v118, v118, v119
	v_cvt_pk_bf16_f32 v119, v174, v175
	v_pk_mul_f32 v[82:83], v[82:83], v[2:3] op_sel_hi:[1,0]
	v_pk_mul_f32 v[80:81], v[80:81], v[2:3] op_sel_hi:[1,0]
	v_pk_mul_f32 v[78:79], v[78:79], v[2:3] op_sel_hi:[1,0]
	v_pk_mul_f32 v[76:77], v[76:77], v[2:3] op_sel_hi:[1,0]
	v_pk_mul_f32 v[74:75], v[74:75], v[2:3] op_sel_hi:[1,0]
	v_pk_mul_f32 v[72:73], v[72:73], v[2:3] op_sel_hi:[1,0]
	v_pk_mul_f32 v[70:71], v[70:71], v[2:3] op_sel_hi:[1,0]
	v_pk_mul_f32 v[68:69], v[68:69], v[2:3] op_sel_hi:[1,0]
	s_waitcnt lgkmcnt(7)
	v_mfma_f32_16x16x32_bf16 v[80:83], v[152:155], v[116:119], v[80:83]
	v_mul_f32_e64 v110, v110, v106
	v_mul_f32_e64 v111, v111, v107
	v_pk_mul_f32 v[108:109], v[108:109], v[104:105]
	v_pk_mul_f32 v[120:121], v[102:103], v[114:115]
	s_waitcnt lgkmcnt(5)
	v_mfma_f32_16x16x32_bf16 v[76:79], v[140:143], v[116:119], v[76:79]
	v_mul_f32_e64 v102, v100, v112
	v_mul_f32_e64 v103, v101, v113
	v_cvt_pk_bf16_f32 v100, v108, v109
	v_cvt_pk_bf16_f32 v101, v110, v111
	s_waitcnt lgkmcnt(3)
	v_mfma_f32_16x16x32_bf16 v[72:75], v[132:135], v[116:119], v[72:75]
	v_cvt_pk_bf16_f32 v102, v102, v103
	v_cvt_pk_bf16_f32 v103, v120, v121
	s_and_b64 vcc, exec, s[42:43]
	s_waitcnt lgkmcnt(1)
	v_mfma_f32_16x16x32_bf16 v[68:71], v[128:131], v[116:119], v[68:71]
	v_mfma_f32_16x16x32_bf16 v[80:83], v[148:151], v[100:103], v[80:83]
	v_mfma_f32_16x16x32_bf16 v[76:79], v[144:147], v[100:103], v[76:79]
	v_mfma_f32_16x16x32_bf16 v[72:75], v[136:139], v[100:103], v[72:75]
	s_waitcnt lgkmcnt(0)
	v_mfma_f32_16x16x32_bf16 v[68:71], v[124:127], v[100:103], v[68:71]
	s_cbranch_vccnz .LBB0_395
	v_cvt_pk_bf16_f32 v100, v104, v105
	v_cvt_pk_bf16_f32 v101, v106, v107
	v_cvt_pk_bf16_f32 v102, v112, v113
	v_cvt_pk_bf16_f32 v103, v114, v115
	v_cvt_pk_bf16_f32 v92, v92, v93
	v_cvt_pk_bf16_f32 v93, v94, v95
	v_cvt_pk_bf16_f32 v94, v96, v97
	v_cvt_pk_bf16_f32 v95, v98, v99
	v_mfma_f32_16x16x32_bf16 v[96:99], v[84:87], v[20:23], 0
	v_mfma_f32_16x16x32_bf16 v[104:107], v[84:87], v[36:39], 0
	v_mfma_f32_16x16x32_bf16 v[108:111], v[84:87], v[44:47], 0
	v_mfma_f32_16x16x32_bf16 v[112:115], v[84:87], v[52:55], 0
	v_mfma_f32_16x16x32_bf16 v[96:99], v[88:91], v[16:19], v[96:99]
	v_mfma_f32_16x16x32_bf16 v[104:107], v[88:91], v[32:35], v[104:107]
	v_mfma_f32_16x16x32_bf16 v[108:111], v[88:91], v[48:51], v[108:111]
	v_mfma_f32_16x16x32_bf16 v[112:115], v[88:91], v[60:63], v[112:115]
	s_nop 4
	v_pk_mul_f32 v[98:99], v[206:207], v[98:99] op_sel_hi:[0,1]
	v_pk_mul_f32 v[96:97], v[206:207], v[96:97] op_sel_hi:[0,1]
	v_pk_mul_f32 v[106:107], v[208:209], v[106:107] op_sel_hi:[0,1]
	v_pk_mul_f32 v[104:105], v[208:209], v[104:105] op_sel_hi:[0,1]
	v_pk_mul_f32 v[110:111], v[210:211], v[110:111] op_sel_hi:[0,1]
	v_pk_mul_f32 v[108:109], v[210:211], v[108:109] op_sel_hi:[0,1]
	v_mul_f32_e64 v114, v212, v114
	v_mul_f32_e64 v115, v212, v115
	v_pk_mul_f32 v[112:113], v[212:213], v[112:113] op_sel_hi:[0,1]
	v_mfma_f32_16x16x32_bf16 v[96:99], v[92:95], v[28:31], v[96:99]
	v_mfma_f32_16x16x32_bf16 v[104:107], v[92:95], v[40:43], v[104:107]
	s_and_b64 vcc, exec, s[44:45]
	s_cbranch_vccz .Lgo_no23
	v_mfma_f32_16x16x32_bf16 v[108:111], v[92:95], v[8:11], v[108:111]
	v_mfma_f32_16x16x32_bf16 v[112:115], v[92:95], v[4:7], v[112:115]
.Lgo_no23:
	v_mfma_f32_16x16x32_bf16 v[108:111], v[100:103], v[56:59], v[108:111]
	v_mfma_f32_16x16x32_bf16 v[112:115], v[100:103], v[64:67], v[112:115]
	s_and_b64 vcc, exec, s[28:29]
	s_cbranch_vccz .LBB0_394
	v_mfma_f32_16x16x32_bf16 v[96:99], v[100:103], v[24:27], v[96:99]
	v_mfma_f32_16x16x32_bf16 v[104:107], v[100:103], v[12:15], v[104:107]
	s_branch .LBB0_394
